# speedup vs baseline: 1.0578x; 1.0396x over previous
.LBB0_17:
	s_andn2_b64 vcc, exec, s[4:5]
	s_cbranch_vccnz .LBB0_21
	s_load_dwordx8 s[4:11], s[0:1], 0x0
	s_load_dwordx4 s[12:15], s[0:1], 0x20
	s_load_dwordx4 s[16:19], s[0:1], 0x50
	s_sub_i32 s20, s2, 0x80
	s_cmpk_ge_i32 s20, 0x90
	s_cselect_b32 s21, 0x90, 0
	s_sub_i32 s20, s20, s21
	s_lshr_b32 s22, s20, 4
	s_and_b32 s23, s20, 15
	s_lshr_b32 s24, s23, 2
	s_and_b32 s25, s23, 3
	v_readfirstlane_b32 s26, v0
	s_lshr_b32 s26, s26, 6
	v_and_b32_e32 v1, 63, v0
	v_and_b32_e32 v2, 31, v1
	v_lshrrev_b32_e32 v3, 5, v1
	v_lshlrev_b32_e32 v4, 9, v2
	v_lshl_add_u32 v4, v3, 4, v4
	s_lshl_b32 s27, s22, 7
	s_lshl_b32 s29, s25, 5
	s_add_u32 s27, s27, s29
	s_lshl_b32 s27, s27, 9
	s_lshl_b32 s29, s26, 5
	s_add_u32 s27, s27, s29
	s_lshl_b32 s28, s24, 14
	s_add_u32 s28, s28, s29
	s_waitcnt lgkmcnt(0)
	s_cmp_lg_u32 s21, 0
	s_cselect_b32 s4, s8, s4
	s_cselect_b32 s5, s9, s5
	s_cselect_b32 s6, s10, s6
	s_cselect_b32 s7, s11, s7
	s_cselect_b32 s12, s14, s12
	s_cselect_b32 s13, s15, s13
	s_cselect_b32 s16, s18, s16
	s_cselect_b32 s17, s19, s17
	s_add_u32 s4, s4, s27
	s_addc_u32 s5, s5, 0
	s_add_u32 s6, s6, s27
	s_addc_u32 s7, s7, 0
	s_add_u32 s12, s12, s28
	s_addc_u32 s13, s13, 0
	global_load_dwordx4 v[8:11], v4, s[4:5]
	global_load_dwordx4 v[12:15], v4, s[6:7]
	global_load_dwordx4 v[40:43], v4, s[12:13]
	s_lshl_b32 s30, s24, 3
	s_add_u32 s30, s30, s25
	s_lshl_b32 s30, s30, 9
	s_lshr_b32 s31, s26, 2
	s_lshl_b32 s31, s31, 7
	s_add_u32 s30, s30, s31
	s_and_b32 s31, s26, 3
	s_add_u32 s30, s30, s31
	s_lshl_b32 s30, s30, 1
	s_lshl_b32 s31, s22, 15
	s_add_u32 s30, s30, s31
	s_add_u32 s16, s16, s30
	s_addc_u32 s17, s17, 0
	v_lshrrev_b32_e32 v6, 4, v2
	v_and_b32_e32 v7, 15, v2
	v_lshlrev_b32_e32 v6, 11, v6
	v_lshl_add_u32 v6, v7, 3, v6
	v_lshl_add_u32 v6, v3, 2, v6
	v_lshlrev_b32_e32 v6, 1, v6
	v_lshlrev_b32_e32 v5, 2, v1
	s_lshl_b32 s30, s26, 12
	v_add_u32_e32 v32, s30, v5
	s_lshl_b32 s30, s26, 8
	v_add_u32_e32 v33, s30, v5
	s_waitcnt vmcnt(1)
	v_pk_add_f32 v[8:9], v[8:9], v[12:13]
	v_pk_add_f32 v[10:11], v[10:11], v[14:15]
	s_waitcnt vmcnt(0)
	s_nop 1
	v_mfma_f32_32x32x2_f32 v[16:31], v8, v40, 0
	v_mfma_f32_32x32x2_f32 v[16:31], v9, v41, v[16:31]
	v_mfma_f32_32x32x2_f32 v[16:31], v10, v42, v[16:31]
	v_mfma_f32_32x32x2_f32 v[16:31], v11, v43, v[16:31]
	s_nop 15
	s_nop 3
	ds_write_b32 v32, v16 offset:0
	ds_write_b32 v32, v17 offset:256
	ds_write_b32 v32, v18 offset:512
	ds_write_b32 v32, v19 offset:768
	ds_write_b32 v32, v20 offset:1024
	ds_write_b32 v32, v21 offset:1280
	ds_write_b32 v32, v22 offset:1536
	ds_write_b32 v32, v23 offset:1792
	ds_write_b32 v32, v24 offset:2048
	ds_write_b32 v32, v25 offset:2304
	ds_write_b32 v32, v26 offset:2560
	ds_write_b32 v32, v27 offset:2816
	ds_write_b32 v32, v28 offset:3072
	ds_write_b32 v32, v29 offset:3328
	ds_write_b32 v32, v30 offset:3584
	ds_write_b32 v32, v31 offset:3840
	s_waitcnt lgkmcnt(0)
	s_barrier
	ds_read_b32 v16, v33 offset:0
	ds_read_b32 v17, v33 offset:4096
	ds_read_b32 v18, v33 offset:8192
	ds_read_b32 v19, v33 offset:12288
	ds_read_b32 v20, v33 offset:16384
	ds_read_b32 v21, v33 offset:20480
	ds_read_b32 v22, v33 offset:24576
	ds_read_b32 v23, v33 offset:28672
	ds_read_b32 v24, v33 offset:32768
	ds_read_b32 v25, v33 offset:36864
	ds_read_b32 v26, v33 offset:40960
	ds_read_b32 v27, v33 offset:45056
	ds_read_b32 v28, v33 offset:49152
	ds_read_b32 v29, v33 offset:53248
	ds_read_b32 v30, v33 offset:57344
	ds_read_b32 v31, v33 offset:61440
	s_waitcnt lgkmcnt(14)
	v_add_f32_e32 v16, v16, v17
	s_waitcnt lgkmcnt(13)
	v_add_f32_e32 v16, v16, v18
	s_waitcnt lgkmcnt(12)
	v_add_f32_e32 v16, v16, v19
	s_waitcnt lgkmcnt(11)
	v_add_f32_e32 v16, v16, v20
	s_waitcnt lgkmcnt(10)
	v_add_f32_e32 v16, v16, v21
	s_waitcnt lgkmcnt(9)
	v_add_f32_e32 v16, v16, v22
	s_waitcnt lgkmcnt(8)
	v_add_f32_e32 v16, v16, v23
	s_waitcnt lgkmcnt(7)
	v_add_f32_e32 v16, v16, v24
	s_waitcnt lgkmcnt(6)
	v_add_f32_e32 v16, v16, v25
	s_waitcnt lgkmcnt(5)
	v_add_f32_e32 v16, v16, v26
	s_waitcnt lgkmcnt(4)
	v_add_f32_e32 v16, v16, v27
	s_waitcnt lgkmcnt(3)
	v_add_f32_e32 v16, v16, v28
	s_waitcnt lgkmcnt(2)
	v_add_f32_e32 v16, v16, v29
	s_waitcnt lgkmcnt(1)
	v_add_f32_e32 v16, v16, v30
	s_waitcnt lgkmcnt(0)
	v_add_f32_e32 v16, v16, v31
	v_cvt_f16_f32_e32 v16, v16
	global_store_short v6, v16, s[16:17]
	s_endpgm

	.amdhsa_kernel _Z6k_prepPKfS0_S0_S0_S0_S0_S0_PKiS2_S2_PtS3_S3_S3_PiS4_S4_S4_S4_S4_
		.amdhsa_group_segment_fixed_size 70144
		.amdhsa_private_segment_fixed_size 0
		.amdhsa_kernarg_size 160
		.amdhsa_user_sgpr_count 2
		.amdhsa_user_sgpr_dispatch_ptr 0
		.amdhsa_user_sgpr_queue_ptr 0
		.amdhsa_user_sgpr_kernarg_segment_ptr 1
		.amdhsa_user_sgpr_dispatch_id 0
		.amdhsa_user_sgpr_kernarg_preload_length 0
		.amdhsa_user_sgpr_kernarg_preload_offset 0
		.amdhsa_user_sgpr_private_segment_size 0
		.amdhsa_uses_dynamic_stack 0
		.amdhsa_enable_private_segment 0
		.amdhsa_system_sgpr_workgroup_id_x 1
		.amdhsa_system_sgpr_workgroup_id_y 0
		.amdhsa_system_sgpr_workgroup_id_z 0
		.amdhsa_system_sgpr_workgroup_info 0
		.amdhsa_system_vgpr_workitem_id 0
		.amdhsa_next_free_vgpr 64
		.amdhsa_next_free_sgpr 40
		.amdhsa_accum_offset 64
		.amdhsa_reserve_vcc 1
		.amdhsa_float_round_mode_32 0
		.amdhsa_float_round_mode_16_64 0
		.amdhsa_float_denorm_mode_32 3
		.amdhsa_float_denorm_mode_16_64 3
		.amdhsa_dx10_clamp 1
		.amdhsa_ieee_mode 1
		.amdhsa_fp16_overflow 0
		.amdhsa_tg_split 0
		.amdhsa_exception_fp_ieee_invalid_op 0
		.amdhsa_exception_fp_denorm_src 0
		.amdhsa_exception_fp_ieee_div_zero 0
		.amdhsa_exception_fp_ieee_overflow 0
		.amdhsa_exception_fp_ieee_underflow 0
		.amdhsa_exception_fp_ieee_inexact 0
		.amdhsa_exception_int_div_zero 0
	.end_amdhsa_kernel

.LBB1_56:
	v_lshrrev_b32_e32 v1, 6, v0
	s_lshl_b32 s2, s2, 4
	s_mov_b32 s12, 0
	v_readfirstlane_b32 s3, v1
	s_mov_b32 s14, 0
	s_or_b32 s2, s2, s3
	s_cmpk_ge_i32 s2, 0xfb2
	s_cbranch_scc1 .LBB1_171
	s_mul_hi_u32 s8, s2, 0x63e7064
	s_mul_i32 s9, s8, 41
	s_sub_i32 s9, s2, s9
	s_lshl_b32 s10, s8, 6
	s_waitcnt lgkmcnt(0)
	s_add_u32 s10, s6, s10
	s_addc_u32 s11, s7, 0
	s_load_dwordx8 s[16:23], s[10:11], 0x0
	s_load_dword s24, s[10:11], 0x20
	v_mov_b32_e32 v6, s8
	v_mov_b32_e32 v39, 0
	s_waitcnt lgkmcnt(0)
	s_mov_b32 s15, s16
	s_add_i32 s13, s15, 31
	s_lshr_b32 s13, s13, 5
	s_cmp_lt_i32 s9, s13
	s_cbranch_scc1 .Lmy_send_found
	s_sub_i32 s9, s9, s13
	s_add_i32 s12, s12, s15
	s_add_i32 s14, s14, 1
	s_mov_b32 s15, s17
	s_add_i32 s13, s15, 31
	s_lshr_b32 s13, s13, 5
	s_cmp_lt_i32 s9, s13
	s_cbranch_scc1 .Lmy_send_found
	s_sub_i32 s9, s9, s13
	s_add_i32 s12, s12, s15
	s_add_i32 s14, s14, 1
	s_mov_b32 s15, s18
	s_add_i32 s13, s15, 31
	s_lshr_b32 s13, s13, 5
	s_cmp_lt_i32 s9, s13
	s_cbranch_scc1 .Lmy_send_found
	s_sub_i32 s9, s9, s13
	s_add_i32 s12, s12, s15
	s_add_i32 s14, s14, 1
	s_mov_b32 s15, s19
	s_add_i32 s13, s15, 31
	s_lshr_b32 s13, s13, 5
	s_cmp_lt_i32 s9, s13
	s_cbranch_scc1 .Lmy_send_found
	s_sub_i32 s9, s9, s13
	s_add_i32 s12, s12, s15
	s_add_i32 s14, s14, 1
	s_mov_b32 s15, s20
	s_add_i32 s13, s15, 31
	s_lshr_b32 s13, s13, 5
	s_cmp_lt_i32 s9, s13
	s_cbranch_scc1 .Lmy_send_found
	s_sub_i32 s9, s9, s13
	s_add_i32 s12, s12, s15
	s_add_i32 s14, s14, 1
	s_mov_b32 s15, s21
	s_add_i32 s13, s15, 31
	s_lshr_b32 s13, s13, 5
	s_cmp_lt_i32 s9, s13
	s_cbranch_scc1 .Lmy_send_found
	s_sub_i32 s9, s9, s13
	s_add_i32 s12, s12, s15
	s_add_i32 s14, s14, 1
	s_mov_b32 s15, s22
	s_add_i32 s13, s15, 31
	s_lshr_b32 s13, s13, 5
	s_cmp_lt_i32 s9, s13
	s_cbranch_scc1 .Lmy_send_found
	s_sub_i32 s9, s9, s13
	s_add_i32 s12, s12, s15
	s_add_i32 s14, s14, 1
	s_mov_b32 s15, s23
	s_add_i32 s13, s15, 31
	s_lshr_b32 s13, s13, 5
	s_cmp_lt_i32 s9, s13
	s_cbranch_scc1 .Lmy_send_found
	s_sub_i32 s9, s9, s13
	s_add_i32 s12, s12, s15
	s_add_i32 s14, s14, 1
	s_mov_b32 s15, s24
	s_add_i32 s13, s15, 31
	s_lshr_b32 s13, s13, 5
	s_cmp_lt_i32 s9, s13
	s_cbranch_scc1 .Lmy_send_found
	s_sub_i32 s9, s9, s13
	s_add_i32 s12, s12, s15
	s_add_i32 s14, s14, 1
	s_branch .LBB1_171
.Lmy_send_found:
	s_lshl_b32 s13, s9, 5
	s_add_i32 s12, s12, s13
	s_sub_i32 s13, s15, s13
	s_min_i32 s13, s13, 32
	s_lshl_b32 s14, s14, 15
	v_mov_b32_e32 v5, s12
	v_mov_b32_e32 v7, s13
	v_mov_b32_e32 v38, s14
	s_load_dwordx4 s[4:7], s[0:1], 0x0
	s_load_dwordx2 s[2:3], s[0:1], 0x20
	v_and_b32_e32 v68, 63, v0
	v_cmp_lt_i32_e32 vcc, v68, v7
	v_mov_b32_e32 v66, -1
	s_and_saveexec_b64 s[8:9], vcc
	s_cbranch_execz .LBB1_76
	s_load_dwordx2 s[0:1], s[0:1], 0x18
	v_lshl_or_b32 v2, v6, 10, v68
	v_add_u32_e32 v2, v2, v5
	v_ashrrev_i32_e32 v3, 31, v2
	s_waitcnt lgkmcnt(0)
	v_lshl_add_u64 v[2:3], v[2:3], 2, s[0:1]
	global_load_dword v66, v[2:3], off
.LBB1_76:
	s_or_b64 exec, exec, s[8:9]
	v_mbcnt_lo_u32_b32 v2, -1, 0
	v_mbcnt_hi_u32_b32 v2, -1, v2
	v_lshrrev_b32_e32 v42, 5, v68
	v_and_b32_e32 v67, 64, v2
	v_lshlrev_b32_e32 v2, 2, v0
	v_and_b32_e32 v43, 0x7c, v2
	v_or_b32_e32 v2, v67, v42
	v_lshlrev_b32_e32 v69, 2, v2
	s_waitcnt vmcnt(0)
	ds_bpermute_b32 v2, v69, v66
	ds_bpermute_b32 v6, v69, v66 offset:8
	ds_bpermute_b32 v10, v69, v66 offset:16
	ds_bpermute_b32 v14, v69, v66 offset:24
	v_lshlrev_b32_e32 v64, 2, v43
	v_mov_b32_e32 v65, 0
	ds_bpermute_b32 v18, v69, v66 offset:32
	s_waitcnt lgkmcnt(0)
	v_lshl_add_u64 v[40:41], s[4:5], 0, v[64:65]
	v_max_i32_e32 v64, 0, v2
	ds_bpermute_b32 v22, v69, v66 offset:40
	v_lshlrev_b64 v[2:3], 9, v[64:65]
	v_max_i32_e32 v64, 0, v6
	ds_bpermute_b32 v26, v69, v66 offset:48
	v_lshlrev_b64 v[6:7], 9, v[64:65]
	v_max_i32_e32 v64, 0, v10
	ds_bpermute_b32 v30, v69, v66 offset:56
	v_lshlrev_b64 v[10:11], 9, v[64:65]
	v_max_i32_e32 v64, 0, v14
	ds_bpermute_b32 v34, v69, v66 offset:64
	v_lshlrev_b64 v[14:15], 9, v[64:65]
	v_max_i32_e32 v64, 0, v18
	ds_bpermute_b32 v44, v69, v66 offset:72
	v_lshlrev_b64 v[18:19], 9, v[64:65]
	s_waitcnt lgkmcnt(4)
	v_max_i32_e32 v64, 0, v22
	ds_bpermute_b32 v48, v69, v66 offset:80
	v_lshlrev_b64 v[22:23], 9, v[64:65]
	s_waitcnt lgkmcnt(4)
	v_max_i32_e32 v64, 0, v26
	ds_bpermute_b32 v52, v69, v66 offset:88
	v_lshlrev_b64 v[26:27], 9, v[64:65]
	s_waitcnt lgkmcnt(4)
	v_max_i32_e32 v64, 0, v30
	ds_bpermute_b32 v56, v69, v66 offset:96
	v_lshlrev_b64 v[30:31], 9, v[64:65]
	s_waitcnt lgkmcnt(4)
	v_max_i32_e32 v64, 0, v34
	ds_bpermute_b32 v60, v69, v66 offset:104
	v_lshlrev_b64 v[34:35], 9, v[64:65]
	s_waitcnt lgkmcnt(4)
	v_max_i32_e32 v64, 0, v44
	ds_bpermute_b32 v70, v69, v66 offset:112
	v_lshl_add_u64 v[2:3], v[40:41], 0, v[2:3]
	v_lshl_add_u64 v[6:7], v[40:41], 0, v[6:7]
	v_lshlrev_b64 v[44:45], 9, v[64:65]
	s_waitcnt lgkmcnt(4)
	v_max_i32_e32 v64, 0, v48
	ds_bpermute_b32 v69, v69, v66 offset:120
	global_load_dwordx4 v[2:5], v[2:3], off nt
	v_lshl_add_u64 v[10:11], v[40:41], 0, v[10:11]
	global_load_dwordx4 v[6:9], v[6:7], off nt
	v_lshl_add_u64 v[14:15], v[40:41], 0, v[14:15]
	v_lshlrev_b64 v[48:49], 9, v[64:65]
	s_waitcnt lgkmcnt(4)
	v_max_i32_e32 v64, 0, v52
	global_load_dwordx4 v[10:13], v[10:11], off nt
	v_lshl_add_u64 v[18:19], v[40:41], 0, v[18:19]
	global_load_dwordx4 v[14:17], v[14:15], off nt
	v_lshl_add_u64 v[22:23], v[40:41], 0, v[22:23]
	v_lshlrev_b64 v[52:53], 9, v[64:65]
	s_waitcnt lgkmcnt(3)
	v_max_i32_e32 v64, 0, v56
	global_load_dwordx4 v[18:21], v[18:19], off nt
	v_lshl_add_u64 v[26:27], v[40:41], 0, v[26:27]
	global_load_dwordx4 v[22:25], v[22:23], off nt
	v_lshl_add_u64 v[30:31], v[40:41], 0, v[30:31]
	v_lshlrev_b64 v[56:57], 9, v[64:65]
	s_waitcnt lgkmcnt(2)
	v_max_i32_e32 v64, 0, v60
	global_load_dwordx4 v[26:29], v[26:27], off nt
	v_lshl_add_u64 v[34:35], v[40:41], 0, v[34:35]
	global_load_dwordx4 v[30:33], v[30:31], off nt
	v_lshl_add_u64 v[44:45], v[40:41], 0, v[44:45]
	v_lshlrev_b64 v[60:61], 9, v[64:65]
	s_waitcnt lgkmcnt(1)
	v_max_i32_e32 v64, 0, v70
	global_load_dwordx4 v[34:37], v[34:35], off nt
	v_lshl_add_u64 v[48:49], v[40:41], 0, v[48:49]
	global_load_dwordx4 v[44:47], v[44:45], off nt
	v_lshl_add_u64 v[52:53], v[40:41], 0, v[52:53]
	v_lshlrev_b64 v[70:71], 9, v[64:65]
	s_waitcnt lgkmcnt(0)
	v_max_i32_e32 v64, 0, v69
	global_load_dwordx4 v[48:51], v[48:49], off nt
	v_lshl_add_u64 v[56:57], v[40:41], 0, v[56:57]
	global_load_dwordx4 v[52:55], v[52:53], off nt
	v_lshl_add_u64 v[60:61], v[40:41], 0, v[60:61]
	v_lshlrev_b64 v[74:75], 9, v[64:65]
	global_load_dwordx4 v[56:59], v[56:57], off nt
	v_lshl_add_u64 v[70:71], v[40:41], 0, v[70:71]
	global_load_dwordx4 v[60:63], v[60:61], off nt
	v_lshl_add_u64 v[40:41], v[40:41], 0, v[74:75]
	global_load_dwordx4 v[70:73], v[70:71], off nt
	v_mul_u32_u24_e32 v69, 0x2200, v1
	global_load_dwordx4 v[74:77], v[40:41], off nt
	s_add_u32 s16, s6, s14
	s_addc_u32 s17, s7, 0
	s_add_u32 s18, s16, 0x1000
	s_addc_u32 s19, s17, 0
	s_add_u32 s20, s16, 0x2000
	s_addc_u32 s21, s17, 0
	s_add_u32 s22, s16, 0x3000
	s_addc_u32 s23, s17, 0
	s_add_u32 s24, s16, 0x4000
	s_addc_u32 s25, s17, 0
	s_add_u32 s26, s16, 0x5000
	s_addc_u32 s27, s17, 0
	s_add_u32 s28, s16, 0x6000
	s_addc_u32 s29, s17, 0
	s_add_u32 s30, s16, 0x7000
	s_addc_u32 s31, s17, 0
	v_and_b32_e32 v116, 63, v0
	v_lshlrev_b32_e32 v116, 4, v116
	global_load_dwordx4 v[84:87], v116, s[16:17]
	global_load_dwordx4 v[88:91], v116, s[18:19]
	global_load_dwordx4 v[92:95], v116, s[20:21]
	global_load_dwordx4 v[96:99], v116, s[22:23]
	global_load_dwordx4 v[100:103], v116, s[24:25]
	global_load_dwordx4 v[104:107], v116, s[26:27]
	global_load_dwordx4 v[108:111], v116, s[28:29]
	global_load_dwordx4 v[112:115], v116, s[30:31]
	v_lshl_or_b32 v40, v43, 1, v69
	s_movk_i32 s4, 0x110
	v_mad_u32_u24 v40, v42, s4, v40
	v_lshlrev_b32_e32 v64, 4, v68
	s_movk_i32 s0, 0x2200
	v_lshrrev_b32_e32 v68, 4, v68
	s_waitcnt vmcnt(23)
	v_cvt_pk_f16_f32 v5, v4, v5
	v_cvt_pk_f16_f32 v4, v2, v3
	s_waitcnt vmcnt(22)
	v_cvt_pk_f16_f32 v3, v8, v9
	v_cvt_pk_f16_f32 v2, v6, v7
	ds_write2_b64 v40, v[4:5], v[2:3] offset1:68
	v_add_u32_e32 v6, 0x800, v40
	s_waitcnt vmcnt(21)
	v_cvt_pk_f16_f32 v3, v12, v13
	v_cvt_pk_f16_f32 v2, v10, v11
	s_waitcnt vmcnt(20)
	v_cvt_pk_f16_f32 v5, v16, v17
	v_cvt_pk_f16_f32 v4, v14, v15
	ds_write2_b64 v40, v[2:3], v[4:5] offset0:136 offset1:204
	s_waitcnt vmcnt(19)
	v_cvt_pk_f16_f32 v3, v20, v21
	v_cvt_pk_f16_f32 v2, v18, v19
	s_waitcnt vmcnt(18)
	v_cvt_pk_f16_f32 v5, v24, v25
	v_cvt_pk_f16_f32 v4, v22, v23
	ds_write2_b64 v6, v[2:3], v[4:5] offset0:16 offset1:84
	s_waitcnt vmcnt(17)
	v_cvt_pk_f16_f32 v3, v28, v29
	v_cvt_pk_f16_f32 v2, v26, v27
	s_waitcnt vmcnt(16)
	v_cvt_pk_f16_f32 v5, v32, v33
	v_cvt_pk_f16_f32 v4, v30, v31
	ds_write2_b64 v6, v[2:3], v[4:5] offset0:152 offset1:220
	v_add_u32_e32 v6, 0x1000, v40
	s_waitcnt vmcnt(15)
	v_cvt_pk_f16_f32 v3, v36, v37
	v_cvt_pk_f16_f32 v2, v34, v35
	s_waitcnt vmcnt(14)
	v_cvt_pk_f16_f32 v5, v46, v47
	v_cvt_pk_f16_f32 v4, v44, v45
	ds_write2_b64 v6, v[2:3], v[4:5] offset0:32 offset1:100
	s_waitcnt vmcnt(13)
	v_cvt_pk_f16_f32 v3, v50, v51
	v_cvt_pk_f16_f32 v2, v48, v49
	s_waitcnt vmcnt(12)
	v_cvt_pk_f16_f32 v5, v54, v55
	v_cvt_pk_f16_f32 v4, v52, v53
	ds_write2_b64 v6, v[2:3], v[4:5] offset0:168 offset1:236
	s_waitcnt vmcnt(11)
	v_cvt_pk_f16_f32 v3, v58, v59
	v_cvt_pk_f16_f32 v2, v56, v57
	s_waitcnt vmcnt(10)
	v_cvt_pk_f16_f32 v5, v62, v63
	v_cvt_pk_f16_f32 v4, v60, v61
	v_add_u32_e32 v6, 0x1800, v40
	ds_write2_b64 v6, v[2:3], v[4:5] offset0:48 offset1:116
	s_waitcnt vmcnt(9)
	v_cvt_pk_f16_f32 v3, v72, v73
	v_cvt_pk_f16_f32 v2, v70, v71
	s_waitcnt vmcnt(8)
	v_cvt_pk_f16_f32 v5, v76, v77
	v_cvt_pk_f16_f32 v4, v74, v75
	ds_write2_b64 v6, v[2:3], v[4:5] offset0:184 offset1:252
	v_lshrrev_b32_e32 v118, 6, v0
	s_movk_i32 s33, 0x110
	v_mul_u32_u24_e32 v117, 0x2200, v118
	v_and_b32_e32 v118, 15, v0
	v_bfe_u32 v119, v0, 4, 2
	v_lshlrev_b32_e32 v67, 4, v118
	v_mad_u32_u24 v121, v119, s33, v117
	v_add_u32_e32 v121, v121, v67
	v_mad_u32_u24 v117, v118, s33, v117
	v_lshl_add_u32 v120, v119, 3, v117
	v_lshl_add_u32 v117, v119, 4, v117
	v_lshlrev_b32_e32 v119, 2, v119
	ds_read_b128 v[68:71], v117
	ds_read_b128 v[72:75], v117 offset:4352
	ds_read_b128 v[76:79], v117 offset:64
	ds_read_b128 v[80:83], v117 offset:4416
	s_waitcnt lgkmcnt(2)
	s_waitcnt vmcnt(7)
	v_mfma_f32_16x16x32_f16 v[2:5], v[84:87], v[68:71], 0
	v_mfma_f32_16x16x32_f16 v[34:37], v[84:87], v[72:75], 0
	global_load_dwordx4 v[84:87], v116, s[16:17] offset:1024
	s_waitcnt vmcnt(7)
	v_mfma_f32_16x16x32_f16 v[6:9], v[88:91], v[68:71], 0
	v_mfma_f32_16x16x32_f16 v[38:41], v[88:91], v[72:75], 0
	global_load_dwordx4 v[88:91], v116, s[18:19] offset:1024
	s_waitcnt vmcnt(7)
	v_mfma_f32_16x16x32_f16 v[10:13], v[92:95], v[68:71], 0
	v_mfma_f32_16x16x32_f16 v[42:45], v[92:95], v[72:75], 0
	global_load_dwordx4 v[92:95], v116, s[20:21] offset:1024
	s_waitcnt vmcnt(7)
	v_mfma_f32_16x16x32_f16 v[14:17], v[96:99], v[68:71], 0
	v_mfma_f32_16x16x32_f16 v[46:49], v[96:99], v[72:75], 0
	global_load_dwordx4 v[96:99], v116, s[22:23] offset:1024
	s_waitcnt vmcnt(7)
	v_mfma_f32_16x16x32_f16 v[18:21], v[100:103], v[68:71], 0
	v_mfma_f32_16x16x32_f16 v[50:53], v[100:103], v[72:75], 0
	global_load_dwordx4 v[100:103], v116, s[24:25] offset:1024
	s_waitcnt vmcnt(7)
	v_mfma_f32_16x16x32_f16 v[22:25], v[104:107], v[68:71], 0
	v_mfma_f32_16x16x32_f16 v[54:57], v[104:107], v[72:75], 0
	global_load_dwordx4 v[104:107], v116, s[26:27] offset:1024
	s_waitcnt vmcnt(7)
	v_mfma_f32_16x16x32_f16 v[26:29], v[108:111], v[68:71], 0
	v_mfma_f32_16x16x32_f16 v[58:61], v[108:111], v[72:75], 0
	global_load_dwordx4 v[108:111], v116, s[28:29] offset:1024
	s_waitcnt vmcnt(7)
	v_mfma_f32_16x16x32_f16 v[30:33], v[112:115], v[68:71], 0
	v_mfma_f32_16x16x32_f16 v[62:65], v[112:115], v[72:75], 0
	global_load_dwordx4 v[112:115], v116, s[30:31] offset:1024
	ds_read_b128 v[68:71], v117 offset:128
	ds_read_b128 v[72:75], v117 offset:4480
	s_waitcnt lgkmcnt(2)
	s_waitcnt vmcnt(7)
	v_mfma_f32_16x16x32_f16 v[2:5], v[84:87], v[76:79], v[2:5]
	v_mfma_f32_16x16x32_f16 v[34:37], v[84:87], v[80:83], v[34:37]
	global_load_dwordx4 v[84:87], v116, s[16:17] offset:2048
	s_waitcnt vmcnt(7)
	v_mfma_f32_16x16x32_f16 v[6:9], v[88:91], v[76:79], v[6:9]
	v_mfma_f32_16x16x32_f16 v[38:41], v[88:91], v[80:83], v[38:41]
	global_load_dwordx4 v[88:91], v116, s[18:19] offset:2048
	s_waitcnt vmcnt(7)
	v_mfma_f32_16x16x32_f16 v[10:13], v[92:95], v[76:79], v[10:13]
	v_mfma_f32_16x16x32_f16 v[42:45], v[92:95], v[80:83], v[42:45]
	global_load_dwordx4 v[92:95], v116, s[20:21] offset:2048
	s_waitcnt vmcnt(7)
	v_mfma_f32_16x16x32_f16 v[14:17], v[96:99], v[76:79], v[14:17]
	v_mfma_f32_16x16x32_f16 v[46:49], v[96:99], v[80:83], v[46:49]
	global_load_dwordx4 v[96:99], v116, s[22:23] offset:2048
	s_waitcnt vmcnt(7)
	v_mfma_f32_16x16x32_f16 v[18:21], v[100:103], v[76:79], v[18:21]
	v_mfma_f32_16x16x32_f16 v[50:53], v[100:103], v[80:83], v[50:53]
	global_load_dwordx4 v[100:103], v116, s[24:25] offset:2048
	s_waitcnt vmcnt(7)
	v_mfma_f32_16x16x32_f16 v[22:25], v[104:107], v[76:79], v[22:25]
	v_mfma_f32_16x16x32_f16 v[54:57], v[104:107], v[80:83], v[54:57]
	global_load_dwordx4 v[104:107], v116, s[26:27] offset:2048
	s_waitcnt vmcnt(7)
	v_mfma_f32_16x16x32_f16 v[26:29], v[108:111], v[76:79], v[26:29]
	v_mfma_f32_16x16x32_f16 v[58:61], v[108:111], v[80:83], v[58:61]
	global_load_dwordx4 v[108:111], v116, s[28:29] offset:2048
	s_waitcnt vmcnt(7)
	v_mfma_f32_16x16x32_f16 v[30:33], v[112:115], v[76:79], v[30:33]
	v_mfma_f32_16x16x32_f16 v[62:65], v[112:115], v[80:83], v[62:65]
	global_load_dwordx4 v[112:115], v116, s[30:31] offset:2048
	ds_read_b128 v[76:79], v117 offset:192
	ds_read_b128 v[80:83], v117 offset:4544
	s_waitcnt lgkmcnt(2)
	s_waitcnt vmcnt(7)
	v_mfma_f32_16x16x32_f16 v[2:5], v[84:87], v[68:71], v[2:5]
	v_mfma_f32_16x16x32_f16 v[34:37], v[84:87], v[72:75], v[34:37]
	global_load_dwordx4 v[84:87], v116, s[16:17] offset:3072
	s_waitcnt vmcnt(7)
	v_mfma_f32_16x16x32_f16 v[6:9], v[88:91], v[68:71], v[6:9]
	v_mfma_f32_16x16x32_f16 v[38:41], v[88:91], v[72:75], v[38:41]
	global_load_dwordx4 v[88:91], v116, s[18:19] offset:3072
	s_waitcnt vmcnt(7)
	v_mfma_f32_16x16x32_f16 v[10:13], v[92:95], v[68:71], v[10:13]
	v_mfma_f32_16x16x32_f16 v[42:45], v[92:95], v[72:75], v[42:45]
	global_load_dwordx4 v[92:95], v116, s[20:21] offset:3072
	s_waitcnt vmcnt(7)
	v_mfma_f32_16x16x32_f16 v[14:17], v[96:99], v[68:71], v[14:17]
	v_mfma_f32_16x16x32_f16 v[46:49], v[96:99], v[72:75], v[46:49]
	global_load_dwordx4 v[96:99], v116, s[22:23] offset:3072
	s_waitcnt vmcnt(7)
	v_mfma_f32_16x16x32_f16 v[18:21], v[100:103], v[68:71], v[18:21]
	v_mfma_f32_16x16x32_f16 v[50:53], v[100:103], v[72:75], v[50:53]
	global_load_dwordx4 v[100:103], v116, s[24:25] offset:3072
	s_waitcnt vmcnt(7)
	v_mfma_f32_16x16x32_f16 v[22:25], v[104:107], v[68:71], v[22:25]
	v_mfma_f32_16x16x32_f16 v[54:57], v[104:107], v[72:75], v[54:57]
	global_load_dwordx4 v[104:107], v116, s[26:27] offset:3072
	s_waitcnt vmcnt(7)
	v_mfma_f32_16x16x32_f16 v[26:29], v[108:111], v[68:71], v[26:29]
	v_mfma_f32_16x16x32_f16 v[58:61], v[108:111], v[72:75], v[58:61]
	global_load_dwordx4 v[108:111], v116, s[28:29] offset:3072
	s_waitcnt vmcnt(7)
	v_mfma_f32_16x16x32_f16 v[30:33], v[112:115], v[68:71], v[30:33]
	v_mfma_f32_16x16x32_f16 v[62:65], v[112:115], v[72:75], v[62:65]
	global_load_dwordx4 v[112:115], v116, s[30:31] offset:3072
	s_waitcnt lgkmcnt(0)
	s_waitcnt vmcnt(7)
	v_mfma_f32_16x16x32_f16 v[2:5], v[84:87], v[76:79], v[2:5]
	v_mfma_f32_16x16x32_f16 v[34:37], v[84:87], v[80:83], v[34:37]
	s_waitcnt vmcnt(6)
	v_mfma_f32_16x16x32_f16 v[6:9], v[88:91], v[76:79], v[6:9]
	v_mfma_f32_16x16x32_f16 v[38:41], v[88:91], v[80:83], v[38:41]
	s_waitcnt vmcnt(5)
	v_mfma_f32_16x16x32_f16 v[10:13], v[92:95], v[76:79], v[10:13]
	v_mfma_f32_16x16x32_f16 v[42:45], v[92:95], v[80:83], v[42:45]
	s_waitcnt vmcnt(4)
	v_mfma_f32_16x16x32_f16 v[14:17], v[96:99], v[76:79], v[14:17]
	v_mfma_f32_16x16x32_f16 v[46:49], v[96:99], v[80:83], v[46:49]
	s_waitcnt vmcnt(3)
	v_mfma_f32_16x16x32_f16 v[18:21], v[100:103], v[76:79], v[18:21]
	v_mfma_f32_16x16x32_f16 v[50:53], v[100:103], v[80:83], v[50:53]
	s_waitcnt vmcnt(2)
	v_mfma_f32_16x16x32_f16 v[22:25], v[104:107], v[76:79], v[22:25]
	v_mfma_f32_16x16x32_f16 v[54:57], v[104:107], v[80:83], v[54:57]
	s_waitcnt vmcnt(1)
	v_mfma_f32_16x16x32_f16 v[26:29], v[108:111], v[76:79], v[26:29]
	v_mfma_f32_16x16x32_f16 v[58:61], v[108:111], v[80:83], v[58:61]
	s_waitcnt vmcnt(0)
	v_mfma_f32_16x16x32_f16 v[30:33], v[112:115], v[76:79], v[30:33]
	v_mfma_f32_16x16x32_f16 v[62:65], v[112:115], v[80:83], v[62:65]
	v_cvt_pk_f16_f32 v2, v2, v3
	v_cvt_pk_f16_f32 v3, v4, v5
	v_cvt_pk_f16_f32 v6, v6, v7
	v_cvt_pk_f16_f32 v7, v8, v9
	v_cvt_pk_f16_f32 v10, v10, v11
	v_cvt_pk_f16_f32 v11, v12, v13
	v_cvt_pk_f16_f32 v14, v14, v15
	v_cvt_pk_f16_f32 v15, v16, v17
	v_cvt_pk_f16_f32 v18, v18, v19
	v_cvt_pk_f16_f32 v19, v20, v21
	v_cvt_pk_f16_f32 v22, v22, v23
	v_cvt_pk_f16_f32 v23, v24, v25
	v_cvt_pk_f16_f32 v26, v26, v27
	v_cvt_pk_f16_f32 v27, v28, v29
	v_cvt_pk_f16_f32 v30, v30, v31
	v_cvt_pk_f16_f32 v31, v32, v33
	v_cvt_pk_f16_f32 v34, v34, v35
	v_cvt_pk_f16_f32 v35, v36, v37
	v_cvt_pk_f16_f32 v38, v38, v39
	v_cvt_pk_f16_f32 v39, v40, v41
	v_cvt_pk_f16_f32 v42, v42, v43
	v_cvt_pk_f16_f32 v43, v44, v45
	v_cvt_pk_f16_f32 v46, v46, v47
	v_cvt_pk_f16_f32 v47, v48, v49
	v_cvt_pk_f16_f32 v50, v50, v51
	v_cvt_pk_f16_f32 v51, v52, v53
	v_cvt_pk_f16_f32 v54, v54, v55
	v_cvt_pk_f16_f32 v55, v56, v57
	v_cvt_pk_f16_f32 v58, v58, v59
	v_cvt_pk_f16_f32 v59, v60, v61
	v_cvt_pk_f16_f32 v62, v62, v63
	v_cvt_pk_f16_f32 v63, v64, v65
	ds_write_b64 v120, v[2:3] offset:0
	ds_write_b64 v120, v[6:7] offset:32
	ds_write_b64 v120, v[10:11] offset:64
	ds_write_b64 v120, v[14:15] offset:96
	ds_write_b64 v120, v[18:19] offset:128
	ds_write_b64 v120, v[22:23] offset:160
	ds_write_b64 v120, v[26:27] offset:192
	ds_write_b64 v120, v[30:31] offset:224
	ds_write_b64 v120, v[34:35] offset:4352
	ds_write_b64 v120, v[38:39] offset:4384
	ds_write_b64 v120, v[42:43] offset:4416
	ds_write_b64 v120, v[46:47] offset:4448
	ds_write_b64 v120, v[50:51] offset:4480
	ds_write_b64 v120, v[54:55] offset:4512
	ds_write_b64 v120, v[58:59] offset:4544
	ds_write_b64 v120, v[62:63] offset:4576
	ds_bpermute_b32 v68, v119, v66 offset:0
	ds_bpermute_b32 v69, v119, v66 offset:16
	ds_bpermute_b32 v70, v119, v66 offset:32
	ds_bpermute_b32 v71, v119, v66 offset:48
	ds_bpermute_b32 v72, v119, v66 offset:64
	ds_bpermute_b32 v73, v119, v66 offset:80
	ds_bpermute_b32 v74, v119, v66 offset:96
	ds_bpermute_b32 v75, v119, v66 offset:112
	ds_read_b128 v[84:87], v121 offset:0
	ds_read_b128 v[88:91], v121 offset:1088
	ds_read_b128 v[92:95], v121 offset:2176
	ds_read_b128 v[96:99], v121 offset:3264
	ds_read_b128 v[100:103], v121 offset:4352
	ds_read_b128 v[104:107], v121 offset:5440
	ds_read_b128 v[108:111], v121 offset:6528
	ds_read_b128 v[112:115], v121 offset:7616
	s_waitcnt lgkmcnt(0)
	v_cmp_lt_i32_e64 s[34:35], -1, v68
	v_lshl_add_u32 v76, v68, 8, v67
	s_mov_b64 exec, s[34:35]
	global_store_dwordx4 v76, v[84:87], s[2:3]
	s_mov_b64 exec, -1
	v_cmp_lt_i32_e64 s[34:35], -1, v69
	v_lshl_add_u32 v77, v69, 8, v67
	s_mov_b64 exec, s[34:35]
	global_store_dwordx4 v77, v[88:91], s[2:3]
	s_mov_b64 exec, -1
	v_cmp_lt_i32_e64 s[34:35], -1, v70
	v_lshl_add_u32 v78, v70, 8, v67
	s_mov_b64 exec, s[34:35]
	global_store_dwordx4 v78, v[92:95], s[2:3]
	s_mov_b64 exec, -1
	v_cmp_lt_i32_e64 s[34:35], -1, v71
	v_lshl_add_u32 v79, v71, 8, v67
	s_mov_b64 exec, s[34:35]
	global_store_dwordx4 v79, v[96:99], s[2:3]
	s_mov_b64 exec, -1
	v_cmp_lt_i32_e64 s[34:35], -1, v72
	v_lshl_add_u32 v80, v72, 8, v67
	s_mov_b64 exec, s[34:35]
	global_store_dwordx4 v80, v[100:103], s[2:3]
	s_mov_b64 exec, -1
	v_cmp_lt_i32_e64 s[34:35], -1, v73
	v_lshl_add_u32 v81, v73, 8, v67
	s_mov_b64 exec, s[34:35]
	global_store_dwordx4 v81, v[104:107], s[2:3]
	s_mov_b64 exec, -1
	v_cmp_lt_i32_e64 s[34:35], -1, v74
	v_lshl_add_u32 v82, v74, 8, v67
	s_mov_b64 exec, s[34:35]
	global_store_dwordx4 v82, v[108:111], s[2:3]
	s_mov_b64 exec, -1
	v_cmp_lt_i32_e64 s[34:35], -1, v75
	v_lshl_add_u32 v83, v75, 8, v67
	s_mov_b64 exec, s[34:35]
	global_store_dwordx4 v83, v[112:115], s[2:3]
	s_mov_b64 exec, -1
	s_endpgm
